# late restore barrier for trailing half, compiler vmcnt(0) dropped, static priority for retention waves 0-3
# speedup vs baseline: 1.0016x; 1.0016x over previous
; #define LAS __attribute__((address_space(3)))
; __device__ __forceinline__ void phase_ret(LAS unsigned char* lds, const bf16* Q, const bf16* Kb, const bf16* V, bf16* Opre, float* stats, int vcu, int G, int tid) {
;     asm volatile("" : "+v"(tid));
;     const int lane = tid & 63, w = __builtin_amdgcn_readfirstlane(tid >> 6), i16 = lane & 15, g4 = lane >> 4;
;     const int ib = (w < 4) ? w : 11 - w;
;     LAS unsigned char* K_t = lds;
;     LAS unsigned char* V_t = lds + 69632;
;     LAS unsigned char* RT_t = lds + 94208;
;     for (int u = vcu; u < BATCH * HEADS * 8; u += G) {
;         const int es = u & 7, h = (u >> 3) & 7, b = u >> 6, hc = h * 256;
;         const float lg2 = log2_gamma(h), gamma_c = __builtin_amdgcn_exp2f(128.0f * lg2);
;         const size_t tb = (size_t)b * SEQ;
;         f32x4 r[2][2];
; #pragma unroll
;         for (int a = 0; a < 2; ++a)
; #pragma unroll
;             for (int c = 0; c < 2; ++c) r[a][c] = (f32x4){0.f, 0.f, 0.f, 0.f};
;         { v4u zz = (v4u){0u, 0u, 0u, 0u}; asm volatile("" : "+v"(zz));
;           int tz = tid; asm volatile("" : "+v"(tz));
;           for (int c = tz; c < 17408 / 16; c += NWAVES * 64) *(LAS v4u*)(RT_t + c * 16) = zz; }
;         v4u kpre[8], vpre;
;         const bf16* kg = Kb + (tb + (tid >> 5)) * LDT + hc + (tid & 31) * 8;
;         const bf16* vg = V + (tb + (tid >> 2)) * LDT + hc + 32 * es + (tid & 3) * 8;
;         const bf16* qg = Q + (tb + 16 * ib + i16) * LDT + hc + 8 * g4;
; #pragma unroll
;         for (int k = 0; k < 8; ++k) kpre[k] = *(const v4u*)(kg + (size_t)k * 16 * LDT);
;         vpre = *(const v4u*)vg;
;         const int i = 16 * ib + i16;
;         bf16x8 qf[8];
; #pragma unroll
;         for (int ks = 0; ks < 8; ++ks) qf[ks] = *(const bf16x8*)(qg + 32 * ks);
.LBB0_419:
	s_or_b64 exec, exec, s[6:7]
	v_readlane_b32 s2, v254, 6
	v_readlane_b32 s3, v254, 7
	v_mov_b32_e32 v152, v212
	s_waitcnt lgkmcnt(0)
	v_cndmask_b32_e64 v3, 0, 1, s[2:3]
	v_cmp_ne_u32_e64 s[4:5], 1, v3
	s_barrier
	s_nop 0
	v_writelane_b32 v255, s4, 53
	s_andn2_b64 vcc, exec, s[2:3]
	v_readfirstlane_b32 s0, v152
	v_writelane_b32 v255, s5, 54
	s_cbranch_vccnz .LBB0_463
	s_ashr_i32 s2, s0, 6
	s_cmp_lt_u32 s2, 4
	s_cbranch_scc0 .Lret_prio_skip
	s_setprio 1
.Lret_prio_skip:
	s_sub_i32 s3, 11, s2
	s_cmp_lt_i32 s2, 4
	s_cselect_b32 s33, s2, s3
	v_bfe_u32 v7, v152, 4, 2
	v_and_b32_e32 v3, 15, v152
	s_lshl_b32 s2, s33, 4
	v_lshlrev_b32_e32 v8, 3, v7
	v_lshlrev_b32_e32 v7, 2, v7
	v_or_b32_e32 v126, s2, v3
	v_or_b32_e32 v18, 49, v7
	v_cmp_gt_i32_e64 s[34:35], v18, v126
	v_or_b32_e32 v18, 50, v7
	v_cmp_gt_i32_e64 s[38:39], v18, v126
	v_or_b32_e32 v18, 51, v7
	v_cmp_gt_i32_e64 s[42:43], v18, v126
	v_or_b32_e32 v18, 0x50, v7
	v_or_b32_e32 v17, 18, v7
	v_cmp_gt_i32_e64 s[46:47], v18, v126
	v_or_b32_e32 v18, 0x41, v7
	v_cmp_gt_i32_e64 s[20:21], v17, v126
	v_or_b32_e32 v17, 19, v7
	v_or_b32_e32 v19, 0x51, v7
	v_cmp_gt_i32_e64 s[48:49], v18, v126
	v_or_b32_e32 v18, 0x42, v7
	v_or_b32_e32 v16, 16, v7
	v_cmp_gt_i32_e64 s[24:25], v17, v126
	v_or_b32_e32 v17, 48, v7
	v_cmp_gt_i32_e64 s[50:51], v19, v126
	v_or_b32_e32 v19, 0x52, v7
	v_cmp_gt_i32_e64 s[52:53], v18, v126
	v_or_b32_e32 v18, 0x43, v7
	v_cmp_gt_i32_e64 s[12:13], v16, v126
	v_or_b32_e32 v16, 17, v7
	v_cmp_gt_i32_e64 s[28:29], v17, v126
	v_or_b32_e32 v17, 33, v7
	v_cmp_gt_i32_e64 s[54:55], v19, v126
	v_or_b32_e32 v19, 0x53, v7
	v_cmp_gt_i32_e64 s[56:57], v18, v126
	v_or_b32_e32 v18, 0x60, v7
	v_ashrrev_i32_e32 v124, 2, v152
	s_ashr_i32 s3, s2, 31
	s_movk_i32 s2, 0x60
	v_cmp_gt_i32_e64 s[16:17], v16, v126
	v_or_b32_e32 v16, 2, v7
	v_cmp_gt_i32_e64 s[30:31], v17, v126
	v_or_b32_e32 v17, 34, v7
	v_cmp_gt_i32_e64 s[58:59], v19, v126
	v_or_b32_e32 v19, 0x70, v7
	v_cmp_gt_i32_e64 s[60:61], v18, v126
	v_or_b32_e32 v18, 0x61, v7
	v_mov_b32_e32 v127, s3
	v_mul_lo_u32 v11, v124, s2
	v_readlane_b32 s3, v255, 34
	v_cmp_gt_i32_e64 s[18:19], v16, v126
	v_or_b32_e32 v16, 3, v7
	v_cmp_gt_i32_e64 s[36:37], v17, v126
	v_or_b32_e32 v17, 35, v7
	v_cmp_gt_i32_e64 s[62:63], v19, v126
	v_or_b32_e32 v19, 0x71, v7
	v_cmp_gt_i32_e64 s[64:65], v18, v126
	v_or_b32_e32 v18, 0x62, v7
	v_and_b32_e32 v5, 63, v152
	v_and_b32_e32 v10, 3, v152
	v_add_u32_e32 v12, s3, v11
	s_min_i32 s80, s33, 3
	v_bfe_u32 v11, v152, 2, 2
	v_cmp_gt_i32_e64 s[22:23], v16, v126
	v_or_b32_e32 v16, 32, v7
	v_cmp_gt_i32_e64 s[40:41], v17, v126
	v_or_b32_e32 v17, 64, v7
	v_cmp_gt_i32_e64 s[66:67], v19, v126
	v_or_b32_e32 v19, 0x72, v7
	v_cmp_gt_i32_e64 s[68:69], v18, v126
	v_or_b32_e32 v18, 0x63, v7
	v_lshlrev_b32_e32 v6, 3, v10
	v_lshlrev_b32_e32 v13, 4, v10
	v_mul_u32_u24_e32 v3, 0x220, v3
	v_and_b32_e32 v10, 48, v152
	s_cmp_gt_i32 s33, 3
	v_lshlrev_b32_e32 v14, 3, v152
	v_cmp_gt_u32_e64 s[8:9], 16, v5
	v_bfe_u32 v5, v152, 2, 4
	v_readlane_b32 s5, v255, 35
	v_cmp_gt_i32_e64 s[10:11], v7, v126
	v_cmp_lt_i32_e64 s[14:15], v7, v126
	v_cmp_gt_i32_e64 s[26:27], v16, v126
	v_cmp_gt_i32_e64 s[70:71], v19, v126
	v_or_b32_e32 v19, 0x73, v7
	v_cmp_gt_i32_e64 s[72:73], v18, v126
	v_or_b32_e32 v7, v7, v11
	v_mov_b32_e32 v18, s3
	v_or_b32_e32 v16, v16, v11
	v_or_b32_e32 v11, v17, v11
	v_add3_u32 v153, 0, v3, v10
	s_cselect_b64 s[6:7], -1, 0
	v_and_b32_e32 v155, 24, v14
	s_andn2_b32 s0, s0, 63
	v_cmp_gt_i32_e64 s[44:45], v17, v126
	v_mad_u32_u24 v7, v7, s2, v18
	v_mad_u32_u24 v16, v16, s2, v18
	v_mad_u32_u24 v156, v5, s2, v18
	v_mad_u32_u24 v17, v11, s2, v18
	v_add3_u32 v157, s5, v10, v3
	v_ashrrev_i32_e32 v11, 31, v126
	v_mov_b32_e32 v10, v126
	v_readlane_b32 s2, v255, 15
	v_or_b32_e32 v14, s0, v155
	s_add_i32 s0, s5, s0
	v_lshlrev_b64 v[10:11], 9, v[10:11]
	v_readlane_b32 s3, v255, 16
	v_add3_u32 v158, s0, v8, v3
	v_lshlrev_b32_e32 v3, 1, v152
	v_lshl_add_u64 v[128:129], s[2:3], 0, v[10:11]
	v_mad_i64_i32 v[10:11], s[2:3], v126, s81, 0
	v_lshrrev_b32_e32 v18, 1, v152
	v_ashrrev_i32_e32 v122, 5, v152
	v_and_b32_e32 v9, 31, v152
	s_movk_i32 s4, 0x220
	v_and_b32_e32 v3, 32, v3
	v_and_b32_e32 v18, 16, v18
	v_readlane_b32 s2, v255, 17
	v_lshlrev_b32_e32 v4, 3, v9
	v_lshl_add_u32 v9, v9, 4, 0
	v_mul_lo_u32 v15, v122, s4
	v_cmp_gt_i32_e64 s[74:75], v19, v126
	v_mad_u32_u24 v19, v5, s4, 0
	v_add_u32_e32 v5, 0xc00, v156
	v_add_u32_e32 v20, 0x1800, v156
	v_add_u32_e32 v21, 0x2400, v156
	v_or3_b32 v10, v10, v3, v18
	v_readlane_b32 s3, v255, 18
	v_ashrrev_i32_e32 v123, 31, v122
	v_ashrrev_i32_e32 v125, 31, v124
	v_add_u32_e32 v154, 0x8800, v153
	v_lshl_add_u64 v[130:131], s[2:3], 0, v[10:11]
	v_lshlrev_b32_e32 v132, 1, v4
	v_lshlrev_b32_e32 v134, 1, v6
	v_lshlrev_b32_e32 v136, 1, v8
	v_add_u32_e32 v159, v9, v15
	v_add_u32_e32 v160, v12, v13
	v_add_u32_e32 v161, v7, v155
	v_add_u32_e32 v162, v16, v155
	v_add_u32_e32 v163, v17, v155
	v_add_u32_e32 v164, v19, v14
	v_add_u32_e32 v165, v5, v155
	v_add_u32_e32 v166, v20, v155
	v_add_u32_e32 v167, v21, v155
	v_readlane_b32 s81, v255, 19
	v_readlane_b32 s2, v252, 17
	v_readlane_b32 s3, v252, 12
	s_branch .LBB0_422

; __device__ __forceinline__ unsigned xb_xcc_id() { return (unsigned)__builtin_amdgcn_s_getreg((3 << 11) | 20) & 0xFu; }
; __device__ __forceinline__ void xcd_barrier(const XcdBarrier& b) {
;     asm volatile("s_waitcnt vmcnt(0)" ::: "memory");
;     __syncthreads();
;     if (threadIdx.x == 0) {
;         unsigned* bar = b.bar; const unsigned bx_ = xb_xcc_id();
;         __builtin_amdgcn_s_waitcnt(0);
;         unsigned nloc = b.st[0], nx = b.st[1];
;         if (nloc == 0u) { xcd_barrier_complete(bar, bx_, nloc, nx); b.st[0] = nloc; b.st[1] = nx; }
.LBB0_463:
	s_setprio 0
	s_waitcnt vmcnt(0)
	s_waitcnt lgkmcnt(0)
	s_barrier
	s_mov_b64 s[6:7], exec
	v_readlane_b32 s2, v252, 15
	v_readlane_b32 s3, v252, 16
	s_and_b64 s[2:3], s[6:7], s[2:3]
	s_mov_b64 exec, s[2:3]
	s_cbranch_execz .LBB0_515
	v_readlane_b32 s2, v255, 32
	s_getreg_b32 s0, hwreg(HW_REG_XCC_ID, 0, 4)
	s_waitcnt vmcnt(0) expcnt(0) lgkmcnt(0)
	v_mov_b32_e32 v3, s2
	ds_read_b32 v5, v3
	v_readlane_b32 s2, v255, 33
	s_and_b32 s0, s0, 15
	s_waitcnt lgkmcnt(0)
	v_cmp_ne_u32_e32 vcc, 0, v5
	v_mov_b32_e32 v3, s2
	ds_read_b32 v4, v3
	s_cbranch_vccnz .LBB0_479
	v_readlane_b32 s4, v252, 8
	v_readlane_b32 s5, v252, 9
	s_load_dwordx2 s[2:3], s[4:5], 0x4
	v_readlane_b32 s4, v252, 10
	v_readlane_b32 s5, v252, 11
	s_waitcnt lgkmcnt(0)
	s_mul_i32 s2, s2, s4
	s_mul_i32 s2, s2, s3
	s_mov_b32 s3, 1
	s_branch .LBB0_467
